# k_g + q-up epilogue: rope cos/sin loads hoisted ahead of the stores (one round trip instead of 8), early vmcnt(0) merged
# baseline (speedup 1.0000x reference)
; #define PG8_LAS __attribute__((address_space(3)))
; __device__ __forceinline__ u32x4 pack8(const f32x4 a, const f32x4 b) { u32x4 w; w.x = cvt_pk_bf16(a[0], a[1]); w.y = cvt_pk_bf16(a[2], a[3]); w.z = cvt_pk_bf16(b[0], b[1]); w.w = cvt_pk_bf16(b[2], b[3]); return w; }
; template <int NP4, int PITCH, int OFF>
; __device__ __forceinline__ void rs_table(const float* part, int rowbase, int wr, int lane, float inv_dim, PG8_LAS float* t) {
;     f32x4 s[2][NP4];
; #pragma unroll
;     for (int ai = 0; ai < 2; ++ai) { const f32x4* p = (const f32x4*)(part + (size_t)(rowbase + ai * 128 + wr * 64 + lane) * PITCH + OFF);
; #pragma unroll
;         for (int j = 0; j < NP4; ++j) s[ai][j] = p[j]; }
; #pragma unroll
;     for (int ai = 0; ai < 2; ++ai) { f32x4 a = s[ai][0];
; #pragma unroll
;         for (int j = 1; j < NP4; ++j) a += s[ai][j];
;         t[ai * 64 + lane] = __builtin_amdgcn_rsqf(((a[0] + a[1]) + (a[2] + a[3])) * inv_dim + 1e-6f); }
;     asm volatile("s_waitcnt lgkmcnt(0)" ::: "memory");
;     __device__ __forceinline__ void operator()(const f32x4 (&acc)[2][2][4][2], const Unit& u, int wr, int wc, int fr, int fq) const {
;         const int lane = fq * 16 + fr, wid = wr * 4 + wc;
;         const float* ssq = (const float*)(ws + WS_SSQ); bf16_t* q = (bf16_t*)(ws + WS_Q); const float* rcos = (const float*)(ws + WS_RCOS); const float* rsin = (const float*)(ws + WS_RSIN);
;         PG8_LAS float* t = tab + wid * 128; rs_table<3, 20, 0>(ssq, u.pm * BM, wr, lane, 1.0f / 384.0f, t);
;         const int row0 = u.pm * BM + wr * 64 + fr;
; #pragma unroll
;         for (int bj = 0; bj < 2; ++bj) {
;             const int colg = u.pn * BM + bj * HALF + wc * 32; const bool rope = ((colg >> 5) % 3) == 2;
; #pragma unroll
;             for (int ai = 0; ai < 2; ++ai)
; #pragma unroll
;                 for (int m = 0; m < 4; ++m) {
;                     const int row = row0 + ai * HALF + m * 16; const float r = t[ai * 64 + m * 16 + fr] * qscale;
;                     f32x4 v0 = acc[ai][bj][m][0] * r, v1 = acc[ai][bj][m][1] * r;
;                     if (rope) rope8(v0, v1, rcos, rsin, row & (SEQ_ - 1), fq);
;                     if (!f8qk) *(u32x4*)(q + (size_t)row * 768 + colg + 8 * fq) = pack8(v0, v1);
;                     if (f8qk) { u32x2 w8; w8.x = pack4_fp8_x16(v0); w8.y = pack4_fp8_x16(v1); *(u32x2*)(ws + WS_Q8 + (size_t)row * 768 + colg + 8 * fq) = w8; }
.LBB0_397:
	s_lshl_b32 s4, s62, 8
	s_add_i32 s28, s4, s53
	v_or_b32_e32 v0, s28, v153
	v_mov_b64_e32 v[148:149], s[20:21]
	s_movk_i32 s29, 0x50
	v_mad_i64_i32 v[168:169], s[4:5], v0, s29, v[148:149]
	global_load_dwordx4 v[158:161], v[168:169], off offset:32
	global_load_dwordx4 v[164:167], v[168:169], off
	s_nop 0
	global_load_dwordx4 v[168:171], v[168:169], off offset:16
	v_add_u32_e32 v0, 0x80, v0
	v_mad_i64_i32 v[148:149], s[4:5], v0, s29, v[148:149]
	global_load_dwordx4 v[172:175], v[148:149], off offset:32
	global_load_dwordx4 v[176:179], v[148:149], off
	global_load_dwordx4 v[180:183], v[148:149], off offset:16
	s_lshl_b32 s4, s61, 8
	s_waitcnt vmcnt(0)
	v_pk_add_f32 v[148:149], v[166:167], v[170:171]
	v_pk_add_f32 v[164:165], v[164:165], v[168:169]
	v_pk_add_f32 v[148:149], v[148:149], v[160:161]
	v_pk_add_f32 v[158:159], v[164:165], v[158:159]
	v_add_f32_e32 v148, v148, v149
	v_add_f32_e32 v0, v158, v159
	v_add_f32_e32 v0, v0, v148
	v_pk_add_f32 v[148:149], v[178:179], v[182:183]
	v_pk_add_f32 v[158:159], v[176:177], v[180:181]
	v_pk_add_f32 v[148:149], v[148:149], v[174:175]
	v_pk_add_f32 v[158:159], v[158:159], v[172:173]
	v_add_f32_e32 v148, v148, v149
	v_add_f32_e32 v157, v158, v159
	v_add_f32_e32 v148, v157, v148
	v_fmamk_f32 v0, v0, 0x3b2aaaab, v248
	v_fmamk_f32 v148, v148, 0x3b2aaaab, v248
	v_rsq_f32_e32 v0, v0
	v_rsq_f32_e32 v148, v148
	v_or_b32_e32 v149, s28, v151
	v_mov_b32_e32 v192, v149
	s_or_b32 s28, s4, s54
	s_ashr_i32 s4, s28, 5
	ds_write2st64_b32 v154, v0, v148 offset1:1
	s_waitcnt lgkmcnt(0)
	s_mul_hi_i32 s5, s4, 0x55555556
	ds_read_b32 v0, v155
	s_lshr_b32 s29, s5, 31
	s_add_i32 s5, s5, s29
	s_mul_i32 s5, s5, 3
	s_sub_i32 s4, s4, s5
	s_cmp_eq_u32 s4, 2
	s_waitcnt lgkmcnt(0)
	v_mul_f32_e32 v148, 0x3e16c740, v0
	v_lshlrev_b32_e32 v0, 6, v149
	s_cselect_b64 s[30:31], -1, 0
	s_cmp_lg_u32 s4, 2
	v_pk_mul_f32 v[124:125], v[124:125], v[148:149] op_sel_hi:[1,0]
	v_pk_mul_f32 v[122:123], v[122:123], v[148:149] op_sel_hi:[1,0]
	v_pk_mul_f32 v[128:129], v[128:129], v[148:149] op_sel_hi:[1,0]
	v_pk_mul_f32 v[126:127], v[126:127], v[148:149] op_sel_hi:[1,0]
	v_and_b32_e32 v0, 0x7f3c0, v0
	s_cbranch_scc1 .LBB0_399
	v_mov_b32_e32 v245, v1
	v_add_u32_e32 v244, 0, v192
	v_lshlrev_b32_e32 v244, 6, v244
	v_and_b32_e32 v244, 0x7ffc0, v244
	v_lshl_add_u64 v[204:205], v[142:143], 0, v[244:245]
	global_load_dwordx4 v[204:207], v[204:205], off
	v_lshl_add_u64 v[208:209], v[140:141], 0, v[244:245]
	global_load_dwordx4 v[208:211], v[208:209], off
	v_add_u32_e32 v244, 16, v192
	v_lshlrev_b32_e32 v244, 6, v244
	v_and_b32_e32 v244, 0x7ffc0, v244
	v_lshl_add_u64 v[212:213], v[142:143], 0, v[244:245]
	global_load_dwordx4 v[212:215], v[212:213], off
	v_lshl_add_u64 v[216:217], v[140:141], 0, v[244:245]
	global_load_dwordx4 v[216:219], v[216:217], off
	v_add_u32_e32 v244, 32, v192
	v_lshlrev_b32_e32 v244, 6, v244
	v_and_b32_e32 v244, 0x7ffc0, v244
	v_lshl_add_u64 v[220:221], v[142:143], 0, v[244:245]
	global_load_dwordx4 v[220:223], v[220:221], off
	v_lshl_add_u64 v[224:225], v[140:141], 0, v[244:245]
	global_load_dwordx4 v[224:227], v[224:225], off
	v_add_u32_e32 v244, 48, v192
	v_lshlrev_b32_e32 v244, 6, v244
	v_and_b32_e32 v244, 0x7ffc0, v244
	v_lshl_add_u64 v[228:229], v[142:143], 0, v[244:245]
	global_load_dwordx4 v[228:231], v[228:229], off
	v_lshl_add_u64 v[232:233], v[140:141], 0, v[244:245]
	global_load_dwordx4 v[232:235], v[232:233], off
	v_add_u32_e32 v244, 128, v192
	v_lshlrev_b32_e32 v244, 6, v244
	v_and_b32_e32 v244, 0x7ffc0, v244
	v_lshl_add_u64 v[236:237], v[142:143], 0, v[244:245]
	global_load_dwordx4 v[236:239], v[236:237], off
	v_lshl_add_u64 v[240:241], v[140:141], 0, v[244:245]
	global_load_dwordx4 v[240:243], v[240:241], off
	v_add_u32_e32 v244, 144, v192
	v_lshlrev_b32_e32 v244, 6, v244
	v_and_b32_e32 v244, 0x7ffc0, v244
	v_lshl_add_u64 v[188:189], v[142:143], 0, v[244:245]
	global_load_dwordx4 v[188:191], v[188:189], off
	v_lshl_add_u64 v[196:197], v[140:141], 0, v[244:245]
	global_load_dwordx4 v[196:199], v[196:197], off
	s_waitcnt vmcnt(0)
	v_pk_mul_f32 v[168:169], v[128:129], v[206:207]
	v_pk_mul_f32 v[170:171], v[126:127], v[204:205]
	v_pk_mul_f32 v[206:207], v[124:125], v[206:207]
	v_pk_mul_f32 v[204:205], v[122:123], v[204:205]
	v_pk_fma_f32 v[124:125], v[124:125], v[210:211], v[168:169] neg_lo:[0,0,1] neg_hi:[0,0,1]
	v_pk_fma_f32 v[122:123], v[122:123], v[208:209], v[170:171] neg_lo:[0,0,1] neg_hi:[0,0,1]
	v_pk_fma_f32 v[128:129], v[128:129], v[210:211], v[206:207]
	v_pk_fma_f32 v[126:127], v[126:127], v[208:209], v[204:205]
; __device__ __forceinline__ u32x4 pack8(const f32x4 a, const f32x4 b) { u32x4 w; w.x = cvt_pk_bf16(a[0], a[1]); w.y = cvt_pk_bf16(a[2], a[3]); w.z = cvt_pk_bf16(b[0], b[1]); w.w = cvt_pk_bf16(b[2], b[3]); return w; }
;     w = __builtin_amdgcn_cvt_pk_fp8_f32(__builtin_amdgcn_fmed3f(v[2] * 16.0f, -448.0f, 448.0f), __builtin_amdgcn_fmed3f(v[3] * 16.0f, -448.0f, 448.0f), w, true); return (unsigned)w; }
;     __device__ __forceinline__ void operator()(const f32x4 (&acc)[2][2][4][2], const Unit& u, int wr, int wc, int fr, int fq) const {
;     ...
;             for (int ai = 0; ai < 2; ++ai)
; #pragma unroll
;                 for (int m = 0; m < 4; ++m) {
;                     const int row = row0 + ai * HALF + m * 16; const float r = t[ai * 64 + m * 16 + fr] * qscale;
;                     f32x4 v0 = acc[ai][bj][m][0] * r, v1 = acc[ai][bj][m][1] * r;
;                     if (rope) rope8(v0, v1, rcos, rsin, row & (SEQ_ - 1), fq);
;                     if (!f8qk) *(u32x4*)(q + (size_t)row * 768 + colg + 8 * fq) = pack8(v0, v1);
;                     if (f8qk) { u32x2 w8; w8.x = pack4_fp8_x16(v0); w8.y = pack4_fp8_x16(v1); *(u32x2*)(ws + WS_Q8 + (size_t)row * 768 + colg + 8 * fq) = w8; }
.LBB0_399:
	v_mul_f32_e32 v122, 0x41800000, v122
	v_med3_f32 v157, v122, s64, v250
	v_mul_f32_e32 v122, 0x41800000, v123
	v_med3_f32 v123, v122, s64, v250
	v_mov_b32_e32 v122, v1
	v_cvt_pk_fp8_f32 v122, v157, v123
	v_mul_f32_e32 v123, 0x41800000, v124
	v_mul_f32_e32 v124, 0x41800000, v125
	v_med3_f32 v123, v123, s64, v250
	v_med3_f32 v124, v124, s64, v250
	v_cvt_pk_fp8_f32 v122, v123, v124 op_sel:[0,0,1]
	v_mul_f32_e32 v123, 0x41800000, v126
	v_med3_f32 v124, v123, s64, v250
	v_mul_f32_e32 v123, 0x41800000, v127
	v_med3_f32 v125, v123, s64, v250
	v_mov_b32_e32 v123, v1
	v_cvt_pk_fp8_f32 v123, v124, v125
	v_mul_f32_e32 v124, 0x41800000, v128
	v_mul_f32_e32 v125, 0x41800000, v129
	v_med3_f32 v124, v124, s64, v250
	v_med3_f32 v125, v125, s64, v250
	ds_read_b32 v126, v155 offset:64
	v_cvt_pk_fp8_f32 v123, v124, v125 op_sel:[0,0,1]
	v_mov_b64_e32 v[124:125], s[22:23]
	s_ashr_i32 s29, s28, 31
	v_mad_i64_i32 v[124:125], s[4:5], v149, s67, v[124:125]
	v_lshl_add_u64 v[124:125], v[124:125], 0, s[28:29]
	v_lshl_add_u64 v[124:125], v[124:125], 0, v[138:139]
	global_store_dwordx2 v[124:125], v[122:123], off
	v_or_b32_e32 v123, 16, v149
	s_waitcnt lgkmcnt(0)
	v_mul_f32_e32 v122, 0x3e16c740, v126
	v_pk_mul_f32 v[126:127], v[116:117], v[122:123] op_sel_hi:[1,0]
	v_cndmask_b32_e64 v116, 0, 1, s[30:31]
	v_cmp_ne_u32_e64 s[4:5], 1, v116
	v_lshlrev_b32_e32 v116, 6, v123
	v_pk_mul_f32 v[120:121], v[120:121], v[122:123] op_sel_hi:[1,0]
	v_pk_mul_f32 v[118:119], v[118:119], v[122:123] op_sel_hi:[1,0]
	v_pk_mul_f32 v[114:115], v[114:115], v[122:123] op_sel_hi:[1,0]
	s_andn2_b64 vcc, exec, s[30:31]
	v_and_b32_e32 v116, 0x7f7c0, v116
	s_cbranch_vccnz .LBB0_401
	v_mov_b32_e32 v117, v1
	v_add_u32_e32 v244, 160, v192
	v_lshlrev_b32_e32 v244, 6, v244
	v_and_b32_e32 v244, 0x7ffc0, v244
	v_lshl_add_u64 v[204:205], v[142:143], 0, v[244:245]
	global_load_dwordx4 v[204:207], v[204:205], off
	v_lshl_add_u64 v[208:209], v[140:141], 0, v[244:245]
	global_load_dwordx4 v[208:211], v[208:209], off
	v_pk_mul_f32 v[128:129], v[126:127], v[214:215]
	v_pk_mul_f32 v[168:169], v[114:115], v[212:213]
	v_pk_mul_f32 v[214:215], v[120:121], v[214:215]
	v_pk_mul_f32 v[212:213], v[118:119], v[212:213]
	v_pk_fma_f32 v[120:121], v[120:121], v[218:219], v[128:129] neg_lo:[0,0,1] neg_hi:[0,0,1]
	v_pk_fma_f32 v[118:119], v[118:119], v[216:217], v[168:169] neg_lo:[0,0,1] neg_hi:[0,0,1]
	v_pk_fma_f32 v[126:127], v[126:127], v[218:219], v[214:215]
	v_pk_fma_f32 v[114:115], v[114:115], v[216:217], v[212:213]
.LBB0_401:
	v_mul_f32_e32 v117, 0x41800000, v118
	v_mul_f32_e32 v118, 0x41800000, v119
	v_med3_f32 v117, v117, s64, v250
	v_med3_f32 v118, v118, s64, v250
	v_mov_b32_e32 v128, v1
	v_cvt_pk_fp8_f32 v128, v117, v118
	v_mul_f32_e32 v114, 0x41800000, v114
	v_mul_f32_e32 v115, 0x41800000, v115
	v_med3_f32 v114, v114, s64, v250
	v_med3_f32 v115, v115, s64, v250
	v_mov_b32_e32 v129, v1
	v_mul_f32_e32 v117, 0x41800000, v120
	v_mul_f32_e32 v118, 0x41800000, v121
	v_cvt_pk_fp8_f32 v129, v114, v115
	v_med3_f32 v117, v117, s64, v250
	v_med3_f32 v118, v118, s64, v250
	v_cvt_pk_fp8_f32 v128, v117, v118 op_sel:[0,0,1]
	v_mul_f32_e32 v114, 0x41800000, v126
	v_mul_f32_e32 v115, 0x41800000, v127
	ds_read_b32 v117, v155 offset:128
	v_med3_f32 v114, v114, s64, v250
	v_med3_f32 v115, v115, s64, v250
	v_cvt_pk_fp8_f32 v129, v114, v115 op_sel:[0,0,1]
	v_mov_b64_e32 v[114:115], s[22:23]
	v_mad_i64_i32 v[114:115], s[30:31], v123, s67, v[114:115]
	v_lshl_add_u64 v[114:115], v[114:115], 0, s[28:29]
	v_lshl_add_u64 v[118:119], v[114:115], 0, v[138:139]
	v_or_b32_e32 v115, 32, v149
	s_waitcnt lgkmcnt(0)
	v_mul_f32_e32 v114, 0x3e16c740, v117
	v_pk_mul_f32 v[120:121], v[108:109], v[114:115] op_sel_hi:[1,0]
	v_lshlrev_b32_e32 v108, 6, v115
	v_pk_mul_f32 v[112:113], v[112:113], v[114:115] op_sel_hi:[1,0]
	v_pk_mul_f32 v[110:111], v[110:111], v[114:115] op_sel_hi:[1,0]
	v_pk_mul_f32 v[106:107], v[106:107], v[114:115] op_sel_hi:[1,0]
	s_and_b64 vcc, exec, s[4:5]
	v_and_b32_e32 v108, 0x7fbc0, v108
	global_store_dwordx2 v[118:119], v[128:129], off
	s_cbranch_vccnz .LBB0_403
	v_mov_b32_e32 v109, v1
	v_add_u32_e32 v244, 176, v192
	v_lshlrev_b32_e32 v244, 6, v244
	v_and_b32_e32 v244, 0x7ffc0, v244
	v_lshl_add_u64 v[212:213], v[142:143], 0, v[244:245]
	global_load_dwordx4 v[212:215], v[212:213], off
	v_lshl_add_u64 v[216:217], v[140:141], 0, v[244:245]
	global_load_dwordx4 v[216:219], v[216:217], off
	v_pk_mul_f32 v[164:165], v[120:121], v[222:223]
	v_pk_mul_f32 v[166:167], v[106:107], v[220:221]
	v_pk_mul_f32 v[222:223], v[112:113], v[222:223]
	v_pk_mul_f32 v[220:221], v[110:111], v[220:221]
	v_pk_fma_f32 v[112:113], v[112:113], v[226:227], v[164:165] neg_lo:[0,0,1] neg_hi:[0,0,1]
	v_pk_fma_f32 v[110:111], v[110:111], v[224:225], v[166:167] neg_lo:[0,0,1] neg_hi:[0,0,1]
	v_pk_fma_f32 v[120:121], v[120:121], v[226:227], v[222:223]
	v_pk_fma_f32 v[106:107], v[106:107], v[224:225], v[220:221]
; __device__ __forceinline__ u32x4 pack8(const f32x4 a, const f32x4 b) { u32x4 w; w.x = cvt_pk_bf16(a[0], a[1]); w.y = cvt_pk_bf16(a[2], a[3]); w.z = cvt_pk_bf16(b[0], b[1]); w.w = cvt_pk_bf16(b[2], b[3]); return w; }
;     w = __builtin_amdgcn_cvt_pk_fp8_f32(__builtin_amdgcn_fmed3f(v[2] * 16.0f, -448.0f, 448.0f), __builtin_amdgcn_fmed3f(v[3] * 16.0f, -448.0f, 448.0f), w, true); return (unsigned)w; }
;     __device__ __forceinline__ void operator()(const f32x4 (&acc)[2][2][4][2], const Unit& u, int wr, int wc, int fr, int fq) const {
;     ...
;             for (int ai = 0; ai < 2; ++ai)
; #pragma unroll
;                 for (int m = 0; m < 4; ++m) {
;                     const int row = row0 + ai * HALF + m * 16; const float r = t[ai * 64 + m * 16 + fr] * qscale;
;                     f32x4 v0 = acc[ai][bj][m][0] * r, v1 = acc[ai][bj][m][1] * r;
;                     if (rope) rope8(v0, v1, rcos, rsin, row & (SEQ_ - 1), fq);
;                     if (!f8qk) *(u32x4*)(q + (size_t)row * 768 + colg + 8 * fq) = pack8(v0, v1);
;                     if (f8qk) { u32x2 w8; w8.x = pack4_fp8_x16(v0); w8.y = pack4_fp8_x16(v1); *(u32x2*)(ws + WS_Q8 + (size_t)row * 768 + colg + 8 * fq) = w8; }
.LBB0_403:
	v_mul_f32_e32 v109, 0x41800000, v110
	v_mul_f32_e32 v110, 0x41800000, v111
	v_med3_f32 v109, v109, s64, v250
	v_med3_f32 v110, v110, s64, v250
	v_mov_b32_e32 v126, v1
	v_cvt_pk_fp8_f32 v126, v109, v110
	v_mul_f32_e32 v106, 0x41800000, v106
	v_mul_f32_e32 v107, 0x41800000, v107
	v_med3_f32 v106, v106, s64, v250
	v_med3_f32 v107, v107, s64, v250
	v_mov_b32_e32 v127, v1
	v_mul_f32_e32 v109, 0x41800000, v112
	v_mul_f32_e32 v110, 0x41800000, v113
	v_cvt_pk_fp8_f32 v127, v106, v107
	v_med3_f32 v109, v109, s64, v250
	v_med3_f32 v110, v110, s64, v250
	v_cvt_pk_fp8_f32 v126, v109, v110 op_sel:[0,0,1]
	v_mul_f32_e32 v106, 0x41800000, v120
	v_mul_f32_e32 v107, 0x41800000, v121
	ds_read_b32 v109, v155 offset:192
	v_med3_f32 v106, v106, s64, v250
	v_med3_f32 v107, v107, s64, v250
	v_cvt_pk_fp8_f32 v127, v106, v107 op_sel:[0,0,1]
	v_mov_b64_e32 v[106:107], s[22:23]
	v_mad_i64_i32 v[106:107], s[30:31], v115, s67, v[106:107]
	v_lshl_add_u64 v[106:107], v[106:107], 0, s[28:29]
	v_lshl_add_u64 v[110:111], v[106:107], 0, v[138:139]
	v_or_b32_e32 v107, 48, v149
	s_waitcnt lgkmcnt(0)
	v_mul_f32_e32 v106, 0x3e16c740, v109
	v_pk_mul_f32 v[112:113], v[100:101], v[106:107] op_sel_hi:[1,0]
	v_lshlrev_b32_e32 v100, 6, v107
	v_pk_mul_f32 v[104:105], v[104:105], v[106:107] op_sel_hi:[1,0]
	v_pk_mul_f32 v[102:103], v[102:103], v[106:107] op_sel_hi:[1,0]
	v_pk_mul_f32 v[98:99], v[98:99], v[106:107] op_sel_hi:[1,0]
	s_and_b64 vcc, exec, s[4:5]
	v_and_b32_e32 v100, 0x7ffc0, v100
	global_store_dwordx2 v[110:111], v[126:127], off
	s_cbranch_vccnz .LBB0_405
	v_mov_b32_e32 v101, v1
	v_pk_mul_f32 v[120:121], v[112:113], v[230:231]
	v_pk_mul_f32 v[164:165], v[98:99], v[228:229]
	v_pk_mul_f32 v[230:231], v[104:105], v[230:231]
	v_pk_mul_f32 v[228:229], v[102:103], v[228:229]
	v_pk_fma_f32 v[104:105], v[104:105], v[234:235], v[120:121] neg_lo:[0,0,1] neg_hi:[0,0,1]
	v_pk_fma_f32 v[102:103], v[102:103], v[232:233], v[164:165] neg_lo:[0,0,1] neg_hi:[0,0,1]
	v_pk_fma_f32 v[112:113], v[112:113], v[234:235], v[230:231]
	v_pk_fma_f32 v[98:99], v[98:99], v[232:233], v[228:229]
.LBB0_405:
	v_mul_f32_e32 v101, 0x41800000, v102
	v_mul_f32_e32 v102, 0x41800000, v103
	v_med3_f32 v101, v101, s64, v250
	v_med3_f32 v102, v102, s64, v250
	v_mov_b32_e32 v120, v1
	v_cvt_pk_fp8_f32 v120, v101, v102
	v_mul_f32_e32 v98, 0x41800000, v98
	v_mul_f32_e32 v99, 0x41800000, v99
	v_med3_f32 v98, v98, s64, v250
	v_med3_f32 v99, v99, s64, v250
	v_mov_b32_e32 v121, v1
	v_mul_f32_e32 v101, 0x41800000, v104
	v_mul_f32_e32 v102, 0x41800000, v105
	v_cvt_pk_fp8_f32 v121, v98, v99
	v_med3_f32 v101, v101, s64, v250
	v_med3_f32 v102, v102, s64, v250
	v_cvt_pk_fp8_f32 v120, v101, v102 op_sel:[0,0,1]
	v_mul_f32_e32 v98, 0x41800000, v112
	v_mul_f32_e32 v99, 0x41800000, v113
	ds_read_b32 v101, v155 offset:256
	v_med3_f32 v98, v98, s64, v250
	v_med3_f32 v99, v99, s64, v250
	v_cvt_pk_fp8_f32 v121, v98, v99 op_sel:[0,0,1]
	v_mov_b64_e32 v[98:99], s[22:23]
	v_mad_i64_i32 v[98:99], s[30:31], v107, s67, v[98:99]
	v_lshl_add_u64 v[98:99], v[98:99], 0, s[28:29]
	v_lshl_add_u64 v[102:103], v[98:99], 0, v[138:139]
	v_add_u32_e32 v99, 0x80, v149
	s_waitcnt lgkmcnt(0)
	v_mul_f32_e32 v98, 0x3e16c740, v101
	v_pk_mul_f32 v[104:105], v[92:93], v[98:99] op_sel_hi:[1,0]
	v_lshlrev_b32_e32 v92, 6, v99
	v_pk_mul_f32 v[96:97], v[96:97], v[98:99] op_sel_hi:[1,0]
	v_pk_mul_f32 v[94:95], v[94:95], v[98:99] op_sel_hi:[1,0]
	v_pk_mul_f32 v[90:91], v[90:91], v[98:99] op_sel_hi:[1,0]
	s_and_b64 vcc, exec, s[4:5]
	v_and_b32_e32 v92, 0x7f3c0, v92
	global_store_dwordx2 v[102:103], v[120:121], off
	s_cbranch_vccnz .LBB0_407
	v_mov_b32_e32 v93, v1
	v_pk_mul_f32 v[112:113], v[104:105], v[238:239]
	v_pk_mul_f32 v[120:121], v[90:91], v[236:237]
	v_pk_mul_f32 v[238:239], v[96:97], v[238:239]
	v_pk_mul_f32 v[236:237], v[94:95], v[236:237]
	v_pk_fma_f32 v[96:97], v[96:97], v[242:243], v[112:113] neg_lo:[0,0,1] neg_hi:[0,0,1]
	v_pk_fma_f32 v[94:95], v[94:95], v[240:241], v[120:121] neg_lo:[0,0,1] neg_hi:[0,0,1]
	v_pk_fma_f32 v[104:105], v[104:105], v[242:243], v[238:239]
	v_pk_fma_f32 v[90:91], v[90:91], v[240:241], v[236:237]
.LBB0_407:
	v_mul_f32_e32 v93, 0x41800000, v94
	v_mul_f32_e32 v94, 0x41800000, v95
	v_med3_f32 v93, v93, s64, v250
	v_med3_f32 v94, v94, s64, v250
	v_mov_b32_e32 v112, v1
	v_cvt_pk_fp8_f32 v112, v93, v94
	v_mul_f32_e32 v90, 0x41800000, v90
	v_mul_f32_e32 v91, 0x41800000, v91
	v_med3_f32 v90, v90, s64, v250
	v_med3_f32 v91, v91, s64, v250
	v_mov_b32_e32 v113, v1
	v_mul_f32_e32 v93, 0x41800000, v96
	v_mul_f32_e32 v94, 0x41800000, v97
	v_cvt_pk_fp8_f32 v113, v90, v91
	v_med3_f32 v93, v93, s64, v250
	v_med3_f32 v94, v94, s64, v250
	v_cvt_pk_fp8_f32 v112, v93, v94 op_sel:[0,0,1]
	v_mul_f32_e32 v90, 0x41800000, v104
	v_mul_f32_e32 v91, 0x41800000, v105
	ds_read_b32 v93, v155 offset:320
	v_med3_f32 v90, v90, s64, v250
	v_med3_f32 v91, v91, s64, v250
	v_cvt_pk_fp8_f32 v113, v90, v91 op_sel:[0,0,1]
	v_mov_b64_e32 v[90:91], s[22:23]
	v_mad_i64_i32 v[90:91], s[30:31], v99, s67, v[90:91]
	v_lshl_add_u64 v[90:91], v[90:91], 0, s[28:29]
	v_lshl_add_u64 v[94:95], v[90:91], 0, v[138:139]
	v_add_u32_e32 v91, 0x90, v149
	s_waitcnt lgkmcnt(0)
	v_mul_f32_e32 v90, 0x3e16c740, v93
	v_pk_mul_f32 v[96:97], v[84:85], v[90:91] op_sel_hi:[1,0]
	v_lshlrev_b32_e32 v84, 6, v91
	v_pk_mul_f32 v[88:89], v[88:89], v[90:91] op_sel_hi:[1,0]
	v_pk_mul_f32 v[86:87], v[86:87], v[90:91] op_sel_hi:[1,0]
	v_pk_mul_f32 v[82:83], v[82:83], v[90:91] op_sel_hi:[1,0]
	s_and_b64 vcc, exec, s[4:5]
	v_and_b32_e32 v84, 0x7f7c0, v84
	global_store_dwordx2 v[94:95], v[112:113], off
	s_cbranch_vccnz .LBB0_409
	v_mov_b32_e32 v85, v1
	v_pk_mul_f32 v[104:105], v[96:97], v[190:191]
	v_pk_mul_f32 v[112:113], v[82:83], v[188:189]
	v_pk_mul_f32 v[120:121], v[88:89], v[190:191]
	v_pk_mul_f32 v[188:189], v[86:87], v[188:189]
	v_pk_fma_f32 v[88:89], v[88:89], v[198:199], v[104:105] neg_lo:[0,0,1] neg_hi:[0,0,1]
	v_pk_fma_f32 v[86:87], v[86:87], v[196:197], v[112:113] neg_lo:[0,0,1] neg_hi:[0,0,1]
	v_pk_fma_f32 v[96:97], v[96:97], v[198:199], v[120:121]
	v_pk_fma_f32 v[82:83], v[82:83], v[196:197], v[188:189]
; __device__ __forceinline__ u32x4 pack8(const f32x4 a, const f32x4 b) { u32x4 w; w.x = cvt_pk_bf16(a[0], a[1]); w.y = cvt_pk_bf16(a[2], a[3]); w.z = cvt_pk_bf16(b[0], b[1]); w.w = cvt_pk_bf16(b[2], b[3]); return w; }
;     __device__ __forceinline__ void operator()(const f32x4 (&acc)[2][2][4][2], const Unit& u, int wr, int wc, int fr, int fq) const {
;     ...
;         for (int bj = 0; bj < 2; ++bj) {
;             const int colg = u.pn * BM + bj * HALF + wc * 32; const bool rope = ((colg >> 5) % 3) == 2;
; #pragma unroll
;             for (int ai = 0; ai < 2; ++ai)
; #pragma unroll
;                 for (int m = 0; m < 4; ++m) {
;                     const int row = row0 + ai * HALF + m * 16; const float r = t[ai * 64 + m * 16 + fr] * qscale;
;                     f32x4 v0 = acc[ai][bj][m][0] * r, v1 = acc[ai][bj][m][1] * r;
;                     if (rope) rope8(v0, v1, rcos, rsin, row & (SEQ_ - 1), fq);
;                     if (!f8qk) *(u32x4*)(q + (size_t)row * 768 + colg + 8 * fq) = pack8(v0, v1);
;                     if (f8qk) { u32x2 w8; w8.x = pack4_fp8_x16(v0); w8.y = pack4_fp8_x16(v1); *(u32x2*)(ws + WS_Q8 + (size_t)row * 768 + colg + 8 * fq) = w8; }
.LBB0_409:
	v_mul_f32_e32 v85, 0x41800000, v86
	v_mul_f32_e32 v86, 0x41800000, v87
	v_med3_f32 v85, v85, s64, v250
	v_med3_f32 v86, v86, s64, v250
	v_mov_b32_e32 v104, v1
	v_cvt_pk_fp8_f32 v104, v85, v86
	v_mul_f32_e32 v82, 0x41800000, v82
	v_mul_f32_e32 v83, 0x41800000, v83
	v_med3_f32 v82, v82, s64, v250
	v_med3_f32 v83, v83, s64, v250
	v_mov_b32_e32 v105, v1
	v_mul_f32_e32 v85, 0x41800000, v88
	v_mul_f32_e32 v86, 0x41800000, v89
	v_cvt_pk_fp8_f32 v105, v82, v83
	v_med3_f32 v85, v85, s64, v250
	v_med3_f32 v86, v86, s64, v250
	v_cvt_pk_fp8_f32 v104, v85, v86 op_sel:[0,0,1]
	v_mul_f32_e32 v82, 0x41800000, v96
	v_mul_f32_e32 v83, 0x41800000, v97
	ds_read_b32 v85, v155 offset:384
	v_med3_f32 v82, v82, s64, v250
	v_med3_f32 v83, v83, s64, v250
	v_cvt_pk_fp8_f32 v105, v82, v83 op_sel:[0,0,1]
	v_mov_b64_e32 v[82:83], s[22:23]
	v_mad_i64_i32 v[82:83], s[30:31], v91, s67, v[82:83]
	v_lshl_add_u64 v[82:83], v[82:83], 0, s[28:29]
	v_lshl_add_u64 v[86:87], v[82:83], 0, v[138:139]
	v_add_u32_e32 v83, 0xa0, v149
	s_waitcnt lgkmcnt(0)
	v_mul_f32_e32 v82, 0x3e16c740, v85
	v_pk_mul_f32 v[88:89], v[76:77], v[82:83] op_sel_hi:[1,0]
	v_lshlrev_b32_e32 v76, 6, v83
	v_pk_mul_f32 v[80:81], v[80:81], v[82:83] op_sel_hi:[1,0]
	v_pk_mul_f32 v[78:79], v[78:79], v[82:83] op_sel_hi:[1,0]
	v_pk_mul_f32 v[74:75], v[74:75], v[82:83] op_sel_hi:[1,0]
	s_and_b64 vcc, exec, s[4:5]
	v_and_b32_e32 v76, 0x7fbc0, v76
	global_store_dwordx2 v[86:87], v[104:105], off
	s_cbranch_vccnz .LBB0_411
	v_mov_b32_e32 v77, v1
	s_waitcnt vmcnt(6)
	v_pk_mul_f32 v[96:97], v[88:89], v[206:207]
	v_pk_mul_f32 v[104:105], v[74:75], v[204:205]
	v_pk_mul_f32 v[112:113], v[80:81], v[206:207]
	v_pk_mul_f32 v[120:121], v[78:79], v[204:205]
	v_pk_fma_f32 v[80:81], v[80:81], v[210:211], v[96:97] neg_lo:[0,0,1] neg_hi:[0,0,1]
	v_pk_fma_f32 v[78:79], v[78:79], v[208:209], v[104:105] neg_lo:[0,0,1] neg_hi:[0,0,1]
	v_pk_fma_f32 v[88:89], v[88:89], v[210:211], v[112:113]
	v_pk_fma_f32 v[74:75], v[74:75], v[208:209], v[120:121]
.LBB0_411:
	v_mul_f32_e32 v77, 0x41800000, v78
	v_mul_f32_e32 v78, 0x41800000, v79
	v_med3_f32 v77, v77, s64, v250
	v_med3_f32 v78, v78, s64, v250
	v_mov_b32_e32 v96, v1
	v_cvt_pk_fp8_f32 v96, v77, v78
	v_mul_f32_e32 v74, 0x41800000, v74
	v_mul_f32_e32 v75, 0x41800000, v75
	v_med3_f32 v74, v74, s64, v250
	v_med3_f32 v75, v75, s64, v250
	v_mov_b32_e32 v97, v1
	v_mul_f32_e32 v77, 0x41800000, v80
	v_mul_f32_e32 v78, 0x41800000, v81
	v_cvt_pk_fp8_f32 v97, v74, v75
	v_med3_f32 v77, v77, s64, v250
	v_med3_f32 v78, v78, s64, v250
	v_cvt_pk_fp8_f32 v96, v77, v78 op_sel:[0,0,1]
	v_mul_f32_e32 v74, 0x41800000, v88
	v_mul_f32_e32 v75, 0x41800000, v89
	ds_read_b32 v77, v155 offset:448
	v_med3_f32 v74, v74, s64, v250
	v_med3_f32 v75, v75, s64, v250
	v_cvt_pk_fp8_f32 v97, v74, v75 op_sel:[0,0,1]
	v_mov_b64_e32 v[74:75], s[22:23]
	v_mad_i64_i32 v[74:75], s[30:31], v83, s67, v[74:75]
	v_lshl_add_u64 v[74:75], v[74:75], 0, s[28:29]
	v_lshl_add_u64 v[78:79], v[74:75], 0, v[138:139]
	v_add_u32_e32 v75, 0xb0, v149
	s_waitcnt lgkmcnt(0)
	v_mul_f32_e32 v74, 0x3e16c740, v77
	v_pk_mul_f32 v[80:81], v[66:67], v[74:75] op_sel_hi:[1,0]
	v_lshlrev_b32_e32 v66, 6, v75
	v_pk_mul_f32 v[72:73], v[72:73], v[74:75] op_sel_hi:[1,0]
	v_pk_mul_f32 v[70:71], v[70:71], v[74:75] op_sel_hi:[1,0]
	v_pk_mul_f32 v[68:69], v[68:69], v[74:75] op_sel_hi:[1,0]
	s_and_b64 vcc, exec, s[4:5]
	v_and_b32_e32 v66, 0x7ffc0, v66
	global_store_dwordx2 v[78:79], v[96:97], off
	s_cbranch_vccnz .LBB0_413
	v_mov_b32_e32 v67, v1
	s_waitcnt vmcnt(4)
	v_pk_mul_f32 v[88:89], v[68:69], v[214:215]
	v_pk_mul_f32 v[96:97], v[80:81], v[212:213]
	v_pk_mul_f32 v[104:105], v[72:73], v[214:215]
	v_pk_mul_f32 v[112:113], v[70:71], v[212:213]
	v_pk_fma_f32 v[72:73], v[72:73], v[218:219], v[88:89] neg_lo:[0,0,1] neg_hi:[0,0,1]
	v_pk_fma_f32 v[70:71], v[70:71], v[216:217], v[96:97] neg_lo:[0,0,1] neg_hi:[0,0,1]
	v_pk_fma_f32 v[68:69], v[68:69], v[218:219], v[104:105]
	v_pk_fma_f32 v[80:81], v[80:81], v[216:217], v[112:113]
.LBB0_413:
	v_mul_f32_e32 v67, 0x41800000, v70
	v_mul_f32_e32 v70, 0x41800000, v71
	v_med3_f32 v67, v67, s64, v250
	v_med3_f32 v71, v70, s64, v250
	v_mov_b32_e32 v70, v1
	v_cvt_pk_fp8_f32 v70, v67, v71
	v_mul_f32_e32 v67, 0x41800000, v72
	v_mul_f32_e32 v71, 0x41800000, v73
	v_med3_f32 v67, v67, s64, v250
	v_med3_f32 v71, v71, s64, v250
	v_cvt_pk_fp8_f32 v70, v67, v71 op_sel:[0,0,1]
	v_mul_f32_e32 v67, 0x41800000, v80
	v_mul_f32_e32 v71, 0x41800000, v81
	v_med3_f32 v67, v67, s64, v250
	v_med3_f32 v72, v71, s64, v250
	v_mov_b32_e32 v71, v1
	v_cvt_pk_fp8_f32 v71, v67, v72
	v_mul_f32_e32 v67, 0x41800000, v68
	v_mul_f32_e32 v68, 0x41800000, v69
	v_med3_f32 v67, v67, s64, v250
	v_med3_f32 v68, v68, s64, v250
	v_cvt_pk_fp8_f32 v71, v67, v68 op_sel:[0,0,1]
	v_mov_b64_e32 v[68:69], s[22:23]
	v_mad_i64_i32 v[68:69], s[4:5], v75, s67, v[68:69]
	s_or_b32 s4, s28, 0x80
	s_ashr_i32 s4, s4, 5
	s_mul_hi_i32 s5, s4, 0x55555556
	v_lshl_add_u64 v[68:69], v[68:69], 0, s[28:29]
	s_lshr_b32 s28, s5, 31
	s_add_i32 s5, s5, s28
	s_mul_i32 s5, s5, 3
	v_lshl_add_u64 v[68:69], v[68:69], 0, v[138:139]
	s_sub_i32 s4, s4, s5
	v_mov_b32_e32 v149, v148
	global_store_dwordx2 v[68:69], v[70:71], off
	s_cmp_eq_u32 s4, 2
	v_mov_b32_e32 v70, v148
	v_mov_b32_e32 v71, v148
	s_cselect_b64 s[28:29], -1, 0
	s_cmp_lg_u32 s4, 2
	v_pk_mul_f32 v[64:65], v[64:65], v[70:71]
	v_pk_mul_f32 v[62:63], v[62:63], v[148:149]
	v_pk_mul_f32 v[60:61], v[60:61], v[70:71]
	v_pk_mul_f32 v[58:59], v[58:59], v[148:149]
	s_cbranch_scc1 .LBB0_415
; __device__ __forceinline__ u32x4 pack8(const f32x4 a, const f32x4 b) { u32x4 w; w.x = cvt_pk_bf16(a[0], a[1]); w.y = cvt_pk_bf16(a[2], a[3]); w.z = cvt_pk_bf16(b[0], b[1]); w.w = cvt_pk_bf16(b[2], b[3]); return w; }
;     __device__ __forceinline__ void operator()(const f32x4 (&acc)[2][2][4][2], const Unit& u, int wr, int wc, int fr, int fq) const {
;     ...
;         for (int bj = 0; bj < 2; ++bj) {
;             const int colg = u.pn * BM + bj * HALF + wc * 32; const bool rope = ((colg >> 5) % 3) == 2;
; #pragma unroll
;             for (int ai = 0; ai < 2; ++ai)
; #pragma unroll
;                 for (int m = 0; m < 4; ++m) {
;                     const int row = row0 + ai * HALF + m * 16; const float r = t[ai * 64 + m * 16 + fr] * qscale;
;                     f32x4 v0 = acc[ai][bj][m][0] * r, v1 = acc[ai][bj][m][1] * r;
;                     if (rope) rope8(v0, v1, rcos, rsin, row & (SEQ_ - 1), fq);
;                     if (!f8qk) *(u32x4*)(q + (size_t)row * 768 + colg + 8 * fq) = pack8(v0, v1);
;                     if (f8qk) { u32x2 w8; w8.x = pack4_fp8_x16(v0); w8.y = pack4_fp8_x16(v1); *(u32x2*)(ws + WS_Q8 + (size_t)row * 768 + colg + 8 * fq) = w8; }
	v_mov_b32_e32 v245, v1
	v_add_u32_e32 v244, 0, v192
	v_lshlrev_b32_e32 v244, 6, v244
	v_and_b32_e32 v244, 0x7ffc0, v244
	v_lshl_add_u64 v[204:205], v[142:143], 0, v[244:245]
	global_load_dwordx4 v[204:207], v[204:205], off
	v_lshl_add_u64 v[208:209], v[140:141], 0, v[244:245]
	global_load_dwordx4 v[208:211], v[208:209], off
	v_add_u32_e32 v244, 16, v192
	v_lshlrev_b32_e32 v244, 6, v244
	v_and_b32_e32 v244, 0x7ffc0, v244
	v_lshl_add_u64 v[212:213], v[142:143], 0, v[244:245]
	global_load_dwordx4 v[212:215], v[212:213], off
	v_lshl_add_u64 v[216:217], v[140:141], 0, v[244:245]
	global_load_dwordx4 v[216:219], v[216:217], off
	v_add_u32_e32 v244, 32, v192
	v_lshlrev_b32_e32 v244, 6, v244
	v_and_b32_e32 v244, 0x7ffc0, v244
	v_lshl_add_u64 v[220:221], v[142:143], 0, v[244:245]
	global_load_dwordx4 v[220:223], v[220:221], off
	v_lshl_add_u64 v[224:225], v[140:141], 0, v[244:245]
	global_load_dwordx4 v[224:227], v[224:225], off
	v_add_u32_e32 v244, 48, v192
	v_lshlrev_b32_e32 v244, 6, v244
	v_and_b32_e32 v244, 0x7ffc0, v244
	v_lshl_add_u64 v[228:229], v[142:143], 0, v[244:245]
	global_load_dwordx4 v[228:231], v[228:229], off
	v_lshl_add_u64 v[232:233], v[140:141], 0, v[244:245]
	global_load_dwordx4 v[232:235], v[232:233], off
	v_add_u32_e32 v244, 128, v192
	v_lshlrev_b32_e32 v244, 6, v244
	v_and_b32_e32 v244, 0x7ffc0, v244
	v_lshl_add_u64 v[236:237], v[142:143], 0, v[244:245]
	global_load_dwordx4 v[236:239], v[236:237], off
	v_lshl_add_u64 v[240:241], v[140:141], 0, v[244:245]
	global_load_dwordx4 v[240:243], v[240:241], off
	v_add_u32_e32 v244, 144, v192
	v_lshlrev_b32_e32 v244, 6, v244
	v_and_b32_e32 v244, 0x7ffc0, v244
	v_lshl_add_u64 v[188:189], v[142:143], 0, v[244:245]
	global_load_dwordx4 v[188:191], v[188:189], off
	v_lshl_add_u64 v[196:197], v[140:141], 0, v[244:245]
	global_load_dwordx4 v[196:199], v[196:197], off
	s_waitcnt vmcnt(0)
	v_pk_mul_f32 v[80:81], v[60:61], v[206:207]
	v_pk_mul_f32 v[88:89], v[58:59], v[204:205]
	v_pk_mul_f32 v[206:207], v[64:65], v[206:207]
	v_pk_mul_f32 v[204:205], v[62:63], v[204:205]
	v_pk_fma_f32 v[64:65], v[64:65], v[210:211], v[80:81] neg_lo:[0,0,1] neg_hi:[0,0,1]
	v_pk_fma_f32 v[62:63], v[62:63], v[208:209], v[88:89] neg_lo:[0,0,1] neg_hi:[0,0,1]
	v_pk_fma_f32 v[60:61], v[60:61], v[210:211], v[206:207]
	v_pk_fma_f32 v[58:59], v[58:59], v[208:209], v[204:205]
.LBB0_415:
	v_mul_f32_e32 v0, 0x41800000, v62
	v_mul_f32_e32 v62, 0x41800000, v63
	v_med3_f32 v0, v0, s64, v250
	v_med3_f32 v63, v62, s64, v250
	v_mov_b32_e32 v62, v1
	v_cvt_pk_fp8_f32 v62, v0, v63
	v_mul_f32_e32 v0, 0x41800000, v64
	v_mul_f32_e32 v63, 0x41800000, v65
	v_med3_f32 v0, v0, s64, v250
	v_med3_f32 v63, v63, s64, v250
	v_cvt_pk_fp8_f32 v62, v0, v63 op_sel:[0,0,1]
	v_mul_f32_e32 v0, 0x41800000, v58
	v_mul_f32_e32 v58, 0x41800000, v59
	v_med3_f32 v0, v0, s64, v250
	v_med3_f32 v58, v58, s64, v250
	v_mov_b32_e32 v63, v1
	v_cvt_pk_fp8_f32 v63, v0, v58
	v_mul_f32_e32 v0, 0x41800000, v60
	v_mul_f32_e32 v58, 0x41800000, v61
	v_med3_f32 v0, v0, s64, v250
	v_med3_f32 v58, v58, s64, v250
	v_cvt_pk_fp8_f32 v63, v0, v58 op_sel:[0,0,1]
	v_mov_b32_e32 v123, v122
	v_mov_b32_e32 v58, v122
	v_mov_b32_e32 v59, v122
	v_cndmask_b32_e64 v0, 0, 1, s[28:29]
	v_pk_mul_f32 v[56:57], v[56:57], v[58:59]
	v_pk_mul_f32 v[54:55], v[54:55], v[122:123]
	v_pk_mul_f32 v[52:53], v[52:53], v[58:59]
	v_cmp_ne_u32_e64 s[4:5], 1, v0
	s_andn2_b64 vcc, exec, s[28:29]
	v_pk_mul_f32 v[50:51], v[50:51], v[122:123]
	global_store_dwordx2 v[124:125], v[62:63], off offset:128
	s_cbranch_vccnz .LBB0_417
	v_mov_b32_e32 v117, v1
	v_add_u32_e32 v244, 160, v192
	v_lshlrev_b32_e32 v244, 6, v244
	v_and_b32_e32 v244, 0x7ffc0, v244
	v_lshl_add_u64 v[204:205], v[142:143], 0, v[244:245]
	global_load_dwordx4 v[204:207], v[204:205], off
	v_lshl_add_u64 v[208:209], v[140:141], 0, v[244:245]
	global_load_dwordx4 v[208:211], v[208:209], off
	v_pk_mul_f32 v[70:71], v[52:53], v[214:215]
	v_pk_mul_f32 v[72:73], v[50:51], v[212:213]
	v_pk_mul_f32 v[214:215], v[56:57], v[214:215]
	v_pk_mul_f32 v[212:213], v[54:55], v[212:213]
	v_pk_fma_f32 v[56:57], v[56:57], v[218:219], v[70:71] neg_lo:[0,0,1] neg_hi:[0,0,1]
	v_pk_fma_f32 v[54:55], v[54:55], v[216:217], v[72:73] neg_lo:[0,0,1] neg_hi:[0,0,1]
	v_pk_fma_f32 v[52:53], v[52:53], v[218:219], v[214:215]
	v_pk_fma_f32 v[50:51], v[50:51], v[216:217], v[212:213]
.LBB0_417:
	v_mul_f32_e32 v0, 0x41800000, v54
	v_mul_f32_e32 v54, 0x41800000, v55
	v_med3_f32 v0, v0, s64, v250
	v_med3_f32 v55, v54, s64, v250
	v_mov_b32_e32 v54, v1
	v_cvt_pk_fp8_f32 v54, v0, v55
	v_mul_f32_e32 v0, 0x41800000, v56
	v_mul_f32_e32 v55, 0x41800000, v57
	v_med3_f32 v0, v0, s64, v250
	v_med3_f32 v55, v55, s64, v250
	v_cvt_pk_fp8_f32 v54, v0, v55 op_sel:[0,0,1]
	v_mul_f32_e32 v0, 0x41800000, v50
	v_mul_f32_e32 v50, 0x41800000, v51
	v_med3_f32 v0, v0, s64, v250
	v_med3_f32 v50, v50, s64, v250
	v_mov_b32_e32 v55, v1
	v_cvt_pk_fp8_f32 v55, v0, v50
	v_mul_f32_e32 v0, 0x41800000, v52
	v_mul_f32_e32 v50, 0x41800000, v53
	v_med3_f32 v0, v0, s64, v250
	v_med3_f32 v50, v50, s64, v250
	v_cvt_pk_fp8_f32 v55, v0, v50 op_sel:[0,0,1]
	v_mov_b32_e32 v115, v114
	v_mov_b32_e32 v50, v114
	v_mov_b32_e32 v51, v114
	v_pk_mul_f32 v[48:49], v[48:49], v[50:51]
	v_pk_mul_f32 v[46:47], v[46:47], v[114:115]
	v_pk_mul_f32 v[44:45], v[44:45], v[50:51]
	s_and_b64 vcc, exec, s[4:5]
	v_pk_mul_f32 v[42:43], v[42:43], v[114:115]
	global_store_dwordx2 v[118:119], v[54:55], off offset:128
	s_cbranch_vccnz .LBB0_419
	v_mov_b32_e32 v109, v1
	v_add_u32_e32 v244, 176, v192
	v_lshlrev_b32_e32 v244, 6, v244
	v_and_b32_e32 v244, 0x7ffc0, v244
	v_lshl_add_u64 v[212:213], v[142:143], 0, v[244:245]
	global_load_dwordx4 v[212:215], v[212:213], off
	v_lshl_add_u64 v[216:217], v[140:141], 0, v[244:245]
	global_load_dwordx4 v[216:219], v[216:217], off
	v_pk_mul_f32 v[58:59], v[44:45], v[222:223]
	v_pk_mul_f32 v[60:61], v[42:43], v[220:221]
	v_pk_mul_f32 v[222:223], v[48:49], v[222:223]
	v_pk_mul_f32 v[220:221], v[46:47], v[220:221]
	v_pk_fma_f32 v[48:49], v[48:49], v[226:227], v[58:59] neg_lo:[0,0,1] neg_hi:[0,0,1]
	v_pk_fma_f32 v[46:47], v[46:47], v[224:225], v[60:61] neg_lo:[0,0,1] neg_hi:[0,0,1]
	v_pk_fma_f32 v[44:45], v[44:45], v[226:227], v[222:223]
	v_pk_fma_f32 v[42:43], v[42:43], v[224:225], v[220:221]
; __device__ __forceinline__ u32x4 pack8(const f32x4 a, const f32x4 b) { u32x4 w; w.x = cvt_pk_bf16(a[0], a[1]); w.y = cvt_pk_bf16(a[2], a[3]); w.z = cvt_pk_bf16(b[0], b[1]); w.w = cvt_pk_bf16(b[2], b[3]); return w; }
;     __device__ __forceinline__ void operator()(const f32x4 (&acc)[2][2][4][2], const Unit& u, int wr, int wc, int fr, int fq) const {
;     ...
;             for (int ai = 0; ai < 2; ++ai)
; #pragma unroll
;                 for (int m = 0; m < 4; ++m) {
;                     const int row = row0 + ai * HALF + m * 16; const float r = t[ai * 64 + m * 16 + fr] * qscale;
;                     f32x4 v0 = acc[ai][bj][m][0] * r, v1 = acc[ai][bj][m][1] * r;
;                     if (rope) rope8(v0, v1, rcos, rsin, row & (SEQ_ - 1), fq);
;                     if (!f8qk) *(u32x4*)(q + (size_t)row * 768 + colg + 8 * fq) = pack8(v0, v1);
;                     if (f8qk) { u32x2 w8; w8.x = pack4_fp8_x16(v0); w8.y = pack4_fp8_x16(v1); *(u32x2*)(ws + WS_Q8 + (size_t)row * 768 + colg + 8 * fq) = w8; }
.LBB0_419:
	v_mul_f32_e32 v0, 0x41800000, v46
	v_mul_f32_e32 v46, 0x41800000, v47
	v_med3_f32 v0, v0, s64, v250
	v_med3_f32 v47, v46, s64, v250
	v_mov_b32_e32 v46, v1
	v_cvt_pk_fp8_f32 v46, v0, v47
	v_mul_f32_e32 v0, 0x41800000, v48
	v_mul_f32_e32 v47, 0x41800000, v49
	v_med3_f32 v0, v0, s64, v250
	v_med3_f32 v47, v47, s64, v250
	v_cvt_pk_fp8_f32 v46, v0, v47 op_sel:[0,0,1]
	v_mul_f32_e32 v0, 0x41800000, v42
	v_mul_f32_e32 v42, 0x41800000, v43
	v_med3_f32 v0, v0, s64, v250
	v_med3_f32 v42, v42, s64, v250
	v_mov_b32_e32 v47, v1
	v_cvt_pk_fp8_f32 v47, v0, v42
	v_mul_f32_e32 v0, 0x41800000, v44
	v_mul_f32_e32 v42, 0x41800000, v45
	v_med3_f32 v0, v0, s64, v250
	v_med3_f32 v42, v42, s64, v250
	v_cvt_pk_fp8_f32 v47, v0, v42 op_sel:[0,0,1]
	v_mov_b32_e32 v107, v106
	v_mov_b32_e32 v42, v106
	v_mov_b32_e32 v43, v106
	v_pk_mul_f32 v[40:41], v[40:41], v[42:43]
	v_pk_mul_f32 v[38:39], v[38:39], v[106:107]
	v_pk_mul_f32 v[36:37], v[36:37], v[42:43]
	s_and_b64 vcc, exec, s[4:5]
	v_pk_mul_f32 v[34:35], v[34:35], v[106:107]
	global_store_dwordx2 v[110:111], v[46:47], off offset:128
	s_cbranch_vccnz .LBB0_421
	v_mov_b32_e32 v101, v1
	v_pk_mul_f32 v[50:51], v[36:37], v[230:231]
	v_pk_mul_f32 v[52:53], v[34:35], v[228:229]
	v_pk_mul_f32 v[230:231], v[40:41], v[230:231]
	v_pk_mul_f32 v[228:229], v[38:39], v[228:229]
	v_pk_fma_f32 v[40:41], v[40:41], v[234:235], v[50:51] neg_lo:[0,0,1] neg_hi:[0,0,1]
	v_pk_fma_f32 v[38:39], v[38:39], v[232:233], v[52:53] neg_lo:[0,0,1] neg_hi:[0,0,1]
	v_pk_fma_f32 v[36:37], v[36:37], v[234:235], v[230:231]
	v_pk_fma_f32 v[34:35], v[34:35], v[232:233], v[228:229]
.LBB0_421:
	v_mul_f32_e32 v0, 0x41800000, v38
	v_mul_f32_e32 v38, 0x41800000, v39
	v_med3_f32 v0, v0, s64, v250
	v_med3_f32 v39, v38, s64, v250
	v_mov_b32_e32 v38, v1
	v_cvt_pk_fp8_f32 v38, v0, v39
	v_mul_f32_e32 v0, 0x41800000, v40
	v_mul_f32_e32 v39, 0x41800000, v41
	v_med3_f32 v0, v0, s64, v250
	v_med3_f32 v39, v39, s64, v250
	v_cvt_pk_fp8_f32 v38, v0, v39 op_sel:[0,0,1]
	v_mul_f32_e32 v0, 0x41800000, v34
	v_mul_f32_e32 v34, 0x41800000, v35
	v_med3_f32 v0, v0, s64, v250
	v_med3_f32 v34, v34, s64, v250
	v_mov_b32_e32 v39, v1
	v_cvt_pk_fp8_f32 v39, v0, v34
	v_mul_f32_e32 v0, 0x41800000, v36
	v_mul_f32_e32 v34, 0x41800000, v37
	v_med3_f32 v0, v0, s64, v250
	v_med3_f32 v34, v34, s64, v250
	v_cvt_pk_fp8_f32 v39, v0, v34 op_sel:[0,0,1]
	v_mov_b32_e32 v99, v98
	v_mov_b32_e32 v34, v98
	v_mov_b32_e32 v35, v98
	v_pk_mul_f32 v[32:33], v[32:33], v[34:35]
	v_pk_mul_f32 v[30:31], v[30:31], v[98:99]
	v_pk_mul_f32 v[28:29], v[28:29], v[34:35]
	s_and_b64 vcc, exec, s[4:5]
	v_pk_mul_f32 v[26:27], v[26:27], v[98:99]
	global_store_dwordx2 v[102:103], v[38:39], off offset:128
	s_cbranch_vccnz .LBB0_423
	v_mov_b32_e32 v93, v1
	v_pk_mul_f32 v[42:43], v[28:29], v[238:239]
	v_pk_mul_f32 v[44:45], v[26:27], v[236:237]
	v_pk_mul_f32 v[238:239], v[32:33], v[238:239]
	v_pk_mul_f32 v[236:237], v[30:31], v[236:237]
	v_pk_fma_f32 v[32:33], v[32:33], v[242:243], v[42:43] neg_lo:[0,0,1] neg_hi:[0,0,1]
	v_pk_fma_f32 v[30:31], v[30:31], v[240:241], v[44:45] neg_lo:[0,0,1] neg_hi:[0,0,1]
	v_pk_fma_f32 v[28:29], v[28:29], v[242:243], v[238:239]
	v_pk_fma_f32 v[26:27], v[26:27], v[240:241], v[236:237]
; __device__ __forceinline__ u32x4 pack8(const f32x4 a, const f32x4 b) { u32x4 w; w.x = cvt_pk_bf16(a[0], a[1]); w.y = cvt_pk_bf16(a[2], a[3]); w.z = cvt_pk_bf16(b[0], b[1]); w.w = cvt_pk_bf16(b[2], b[3]); return w; }
;     __device__ __forceinline__ void operator()(const f32x4 (&acc)[2][2][4][2], const Unit& u, int wr, int wc, int fr, int fq) const {
;     ...
;             for (int ai = 0; ai < 2; ++ai)
; #pragma unroll
;                 for (int m = 0; m < 4; ++m) {
;                     const int row = row0 + ai * HALF + m * 16; const float r = t[ai * 64 + m * 16 + fr] * qscale;
;                     f32x4 v0 = acc[ai][bj][m][0] * r, v1 = acc[ai][bj][m][1] * r;
;                     if (rope) rope8(v0, v1, rcos, rsin, row & (SEQ_ - 1), fq);
;                     if (!f8qk) *(u32x4*)(q + (size_t)row * 768 + colg + 8 * fq) = pack8(v0, v1);
;                     if (f8qk) { u32x2 w8; w8.x = pack4_fp8_x16(v0); w8.y = pack4_fp8_x16(v1); *(u32x2*)(ws + WS_Q8 + (size_t)row * 768 + colg + 8 * fq) = w8; }
.LBB0_423:
	v_mul_f32_e32 v0, 0x41800000, v30
	v_mul_f32_e32 v30, 0x41800000, v31
	v_med3_f32 v0, v0, s64, v250
	v_med3_f32 v31, v30, s64, v250
	v_mov_b32_e32 v30, v1
	v_cvt_pk_fp8_f32 v30, v0, v31
	v_mul_f32_e32 v0, 0x41800000, v32
	v_mul_f32_e32 v31, 0x41800000, v33
	v_med3_f32 v0, v0, s64, v250
	v_med3_f32 v31, v31, s64, v250
	v_cvt_pk_fp8_f32 v30, v0, v31 op_sel:[0,0,1]
	v_mul_f32_e32 v0, 0x41800000, v26
	v_mul_f32_e32 v26, 0x41800000, v27
	v_med3_f32 v0, v0, s64, v250
	v_med3_f32 v26, v26, s64, v250
	v_mov_b32_e32 v31, v1
	v_cvt_pk_fp8_f32 v31, v0, v26
	v_mul_f32_e32 v0, 0x41800000, v28
	v_mul_f32_e32 v26, 0x41800000, v29
	v_med3_f32 v0, v0, s64, v250
	v_med3_f32 v26, v26, s64, v250
	v_cvt_pk_fp8_f32 v31, v0, v26 op_sel:[0,0,1]
	v_mov_b32_e32 v91, v90
	v_mov_b32_e32 v26, v90
	v_mov_b32_e32 v27, v90
	v_pk_mul_f32 v[24:25], v[24:25], v[26:27]
	v_pk_mul_f32 v[22:23], v[22:23], v[90:91]
	v_pk_mul_f32 v[20:21], v[20:21], v[26:27]
	s_and_b64 vcc, exec, s[4:5]
	v_pk_mul_f32 v[18:19], v[18:19], v[90:91]
	global_store_dwordx2 v[94:95], v[30:31], off offset:128
	s_cbranch_vccnz .LBB0_425
	v_mov_b32_e32 v85, v1
	v_pk_mul_f32 v[34:35], v[20:21], v[190:191]
	v_pk_mul_f32 v[36:37], v[18:19], v[188:189]
	v_pk_mul_f32 v[190:191], v[24:25], v[190:191]
	v_pk_mul_f32 v[188:189], v[22:23], v[188:189]
	v_pk_fma_f32 v[24:25], v[24:25], v[198:199], v[34:35] neg_lo:[0,0,1] neg_hi:[0,0,1]
	v_pk_fma_f32 v[22:23], v[22:23], v[196:197], v[36:37] neg_lo:[0,0,1] neg_hi:[0,0,1]
	v_pk_fma_f32 v[20:21], v[20:21], v[198:199], v[190:191]
	v_pk_fma_f32 v[18:19], v[18:19], v[196:197], v[188:189]
.LBB0_425:
	v_mul_f32_e32 v0, 0x41800000, v22
	v_mul_f32_e32 v22, 0x41800000, v23
	v_med3_f32 v0, v0, s64, v250
	v_med3_f32 v23, v22, s64, v250
	v_mov_b32_e32 v22, v1
	v_cvt_pk_fp8_f32 v22, v0, v23
	v_mul_f32_e32 v0, 0x41800000, v24
	v_mul_f32_e32 v23, 0x41800000, v25
	v_med3_f32 v0, v0, s64, v250
	v_med3_f32 v23, v23, s64, v250
	v_cvt_pk_fp8_f32 v22, v0, v23 op_sel:[0,0,1]
	v_mul_f32_e32 v0, 0x41800000, v18
	v_mul_f32_e32 v18, 0x41800000, v19
	v_med3_f32 v0, v0, s64, v250
	v_med3_f32 v18, v18, s64, v250
	v_mov_b32_e32 v23, v1
	v_cvt_pk_fp8_f32 v23, v0, v18
	v_mul_f32_e32 v0, 0x41800000, v20
	v_mul_f32_e32 v18, 0x41800000, v21
	v_med3_f32 v0, v0, s64, v250
	v_med3_f32 v18, v18, s64, v250
	v_cvt_pk_fp8_f32 v23, v0, v18 op_sel:[0,0,1]
	v_mov_b32_e32 v83, v82
	v_mov_b32_e32 v18, v82
	v_mov_b32_e32 v19, v82
	v_pk_mul_f32 v[16:17], v[16:17], v[18:19]
	v_pk_mul_f32 v[14:15], v[14:15], v[82:83]
	v_pk_mul_f32 v[12:13], v[12:13], v[18:19]
	s_and_b64 vcc, exec, s[4:5]
	v_pk_mul_f32 v[10:11], v[10:11], v[82:83]
	global_store_dwordx2 v[86:87], v[22:23], off offset:128
	s_cbranch_vccnz .LBB0_427
	v_mov_b32_e32 v77, v1
	s_waitcnt vmcnt(6)
	v_pk_mul_f32 v[26:27], v[12:13], v[206:207]
	v_pk_mul_f32 v[28:29], v[10:11], v[204:205]
	v_pk_mul_f32 v[206:207], v[16:17], v[206:207]
	v_pk_mul_f32 v[204:205], v[14:15], v[204:205]
	v_pk_fma_f32 v[16:17], v[16:17], v[210:211], v[26:27] neg_lo:[0,0,1] neg_hi:[0,0,1]
	v_pk_fma_f32 v[14:15], v[14:15], v[208:209], v[28:29] neg_lo:[0,0,1] neg_hi:[0,0,1]
	v_pk_fma_f32 v[12:13], v[12:13], v[210:211], v[206:207]
	v_pk_fma_f32 v[10:11], v[10:11], v[208:209], v[204:205]
.LBB0_427:
	v_mul_f32_e32 v0, 0x41800000, v14
	v_mul_f32_e32 v14, 0x41800000, v15
	v_med3_f32 v0, v0, s64, v250
	v_med3_f32 v15, v14, s64, v250
	v_mov_b32_e32 v14, v1
	v_cvt_pk_fp8_f32 v14, v0, v15
	v_mul_f32_e32 v0, 0x41800000, v16
	v_mul_f32_e32 v15, 0x41800000, v17
	v_med3_f32 v0, v0, s64, v250
	v_med3_f32 v15, v15, s64, v250
	v_cvt_pk_fp8_f32 v14, v0, v15 op_sel:[0,0,1]
	v_mul_f32_e32 v0, 0x41800000, v10
	v_mul_f32_e32 v10, 0x41800000, v11
	v_med3_f32 v0, v0, s64, v250
	v_med3_f32 v10, v10, s64, v250
	v_mov_b32_e32 v15, v1
	v_cvt_pk_fp8_f32 v15, v0, v10
	v_mul_f32_e32 v0, 0x41800000, v12
	v_mul_f32_e32 v10, 0x41800000, v13
	v_med3_f32 v0, v0, s64, v250
	v_med3_f32 v10, v10, s64, v250
	v_cvt_pk_fp8_f32 v15, v0, v10 op_sel:[0,0,1]
	v_mov_b32_e32 v75, v74
	v_mov_b32_e32 v10, v74
	v_mov_b32_e32 v11, v74
	v_pk_mul_f32 v[8:9], v[8:9], v[10:11]
	v_pk_mul_f32 v[6:7], v[6:7], v[74:75]
	v_pk_mul_f32 v[4:5], v[4:5], v[10:11]
	s_and_b64 vcc, exec, s[4:5]
	v_pk_mul_f32 v[2:3], v[2:3], v[74:75]
	global_store_dwordx2 v[78:79], v[14:15], off offset:128
	s_cbranch_vccnz .LBB0_429
	v_mov_b32_e32 v67, v1
	s_waitcnt vmcnt(4)
	v_pk_mul_f32 v[18:19], v[4:5], v[214:215]
	v_pk_mul_f32 v[20:21], v[2:3], v[212:213]
	v_pk_mul_f32 v[214:215], v[8:9], v[214:215]
	v_pk_mul_f32 v[212:213], v[6:7], v[212:213]
	v_pk_fma_f32 v[8:9], v[8:9], v[218:219], v[18:19] neg_lo:[0,0,1] neg_hi:[0,0,1]
	v_pk_fma_f32 v[6:7], v[6:7], v[216:217], v[20:21] neg_lo:[0,0,1] neg_hi:[0,0,1]
	v_pk_fma_f32 v[4:5], v[4:5], v[218:219], v[214:215]
	v_pk_fma_f32 v[2:3], v[2:3], v[216:217], v[212:213]
